# acc zeroing via v_mov_b64 (64 instr instead of 128 v_mov_b32) in P1 P4 P7 P8 unit loops
# speedup vs baseline: 1.0018x; 1.0007x over previous
.LBB0_122:
	s_ashr_i32 s7, s6, 31
	s_lshl_b64 s[42:43], s[6:7], 18
	s_add_u32 s48, s53, s42
	s_addc_u32 s49, s54, s43
	s_and_b64 s[42:43], s[58:59], exec
	s_cselect_b32 s2, s49, s41
	s_cselect_b32 s7, s48, s40
	s_lshl_b32 s50, s37, 8
	s_or_b32 s51, s50, 0x80
	s_add_u32 s56, s40, 0x100
	s_addc_u32 s57, s41, 0
	s_mov_b32 s60, -2
	s_mov_b64 s[62:63], s[26:27]
	v_mov_b64_e32 v[90:91], 0
	v_mov_b64_e32 v[92:93], 0
	v_mov_b64_e32 v[94:95], 0
	v_mov_b64_e32 v[96:97], 0
	v_mov_b64_e32 v[114:115], 0
	v_mov_b64_e32 v[116:117], 0
	v_mov_b64_e32 v[118:119], 0
	v_mov_b64_e32 v[120:121], 0
	v_mov_b64_e32 v[66:67], 0
	v_mov_b64_e32 v[68:69], 0
	v_mov_b64_e32 v[70:71], 0
	v_mov_b64_e32 v[72:73], 0
	v_mov_b64_e32 v[74:75], 0
	v_mov_b64_e32 v[76:77], 0
	v_mov_b64_e32 v[78:79], 0
	v_mov_b64_e32 v[80:81], 0
	v_mov_b64_e32 v[106:107], 0
	v_mov_b64_e32 v[108:109], 0
	v_mov_b64_e32 v[110:111], 0
	v_mov_b64_e32 v[112:113], 0
	v_mov_b64_e32 v[122:123], 0
	v_mov_b64_e32 v[124:125], 0
	v_mov_b64_e32 v[126:127], 0
	v_mov_b64_e32 v[128:129], 0
	v_mov_b64_e32 v[130:131], 0
	v_mov_b64_e32 v[132:133], 0
	v_mov_b64_e32 v[134:135], 0
	v_mov_b64_e32 v[136:137], 0
	v_mov_b64_e32 v[146:147], 0
	v_mov_b64_e32 v[148:149], 0
	v_mov_b64_e32 v[150:151], 0
	v_mov_b64_e32 v[152:153], 0
	v_mov_b64_e32 v[162:163], 0
	v_mov_b64_e32 v[164:165], 0
	v_mov_b64_e32 v[166:167], 0
	v_mov_b64_e32 v[168:169], 0
	v_mov_b64_e32 v[178:179], 0
	v_mov_b64_e32 v[180:181], 0
	v_mov_b64_e32 v[182:183], 0
	v_mov_b64_e32 v[184:185], 0
	v_mov_b64_e32 v[138:139], 0
	v_mov_b64_e32 v[140:141], 0
	v_mov_b64_e32 v[142:143], 0
	v_mov_b64_e32 v[144:145], 0
	v_mov_b64_e32 v[154:155], 0
	v_mov_b64_e32 v[156:157], 0
	v_mov_b64_e32 v[158:159], 0
	v_mov_b64_e32 v[160:161], 0
	v_mov_b64_e32 v[170:171], 0
	v_mov_b64_e32 v[172:173], 0
	v_mov_b64_e32 v[174:175], 0
	v_mov_b64_e32 v[176:177], 0
	v_mov_b64_e32 v[186:187], 0
	v_mov_b64_e32 v[188:189], 0
	v_mov_b64_e32 v[190:191], 0
	v_mov_b64_e32 v[192:193], 0
	v_mov_b64_e32 v[98:99], 0
	v_mov_b64_e32 v[100:101], 0
	v_mov_b64_e32 v[102:103], 0
	v_mov_b64_e32 v[104:105], 0
	v_mov_b64_e32 v[82:83], 0
	v_mov_b64_e32 v[84:85], 0
	v_mov_b64_e32 v[86:87], 0
	v_mov_b64_e32 v[88:89], 0
	s_mov_b32 s61, 1
	s_branch .LBB0_124

.LBB0_569:
	s_ashr_i32 s9, s8, 31
	s_lshl_b64 s[30:31], s[8:9], 18
	s_add_u32 s30, s33, s30
	s_addc_u32 s31, s46, s31
	s_and_b64 s[40:41], s[36:37], exec
	s_cselect_b32 s2, s31, s39
	s_cselect_b32 s9, s30, s38
	s_lshl_b32 s35, s27, 8
	s_or_b32 s63, s35, 0x80
	s_add_u32 s64, s38, 0x100
	s_addc_u32 s65, s39, 0
	s_mov_b32 s66, -2
	s_mov_b64 s[38:39], s[18:19]
	v_mov_b64_e32 v[90:91], 0
	v_mov_b64_e32 v[92:93], 0
	v_mov_b64_e32 v[102:103], 0
	v_mov_b64_e32 v[104:105], 0
	s_waitcnt vmcnt(0)
	v_mov_b64_e32 v[114:115], 0
	v_mov_b64_e32 v[116:117], 0
	v_mov_b64_e32 v[118:119], 0
	v_mov_b64_e32 v[120:121], 0
	v_mov_b64_e32 v[66:67], 0
	v_mov_b64_e32 v[68:69], 0
	v_mov_b64_e32 v[70:71], 0
	v_mov_b64_e32 v[72:73], 0
	v_mov_b64_e32 v[82:83], 0
	v_mov_b64_e32 v[84:85], 0
	v_mov_b64_e32 v[86:87], 0
	v_mov_b64_e32 v[88:89], 0
	v_mov_b64_e32 v[106:107], 0
	v_mov_b64_e32 v[108:109], 0
	v_mov_b64_e32 v[110:111], 0
	v_mov_b64_e32 v[112:113], 0
	v_mov_b64_e32 v[122:123], 0
	v_mov_b64_e32 v[124:125], 0
	v_mov_b64_e32 v[126:127], 0
	v_mov_b64_e32 v[128:129], 0
	v_mov_b64_e32 v[130:131], 0
	v_mov_b64_e32 v[132:133], 0
	v_mov_b64_e32 v[134:135], 0
	v_mov_b64_e32 v[136:137], 0
	v_mov_b64_e32 v[146:147], 0
	v_mov_b64_e32 v[148:149], 0
	v_mov_b64_e32 v[150:151], 0
	v_mov_b64_e32 v[152:153], 0
	v_mov_b64_e32 v[162:163], 0
	v_mov_b64_e32 v[164:165], 0
	v_mov_b64_e32 v[166:167], 0
	v_mov_b64_e32 v[168:169], 0
	v_mov_b64_e32 v[178:179], 0
	v_mov_b64_e32 v[180:181], 0
	v_mov_b64_e32 v[182:183], 0
	v_mov_b64_e32 v[184:185], 0
	v_mov_b64_e32 v[138:139], 0
	v_mov_b64_e32 v[140:141], 0
	v_mov_b64_e32 v[142:143], 0
	v_mov_b64_e32 v[144:145], 0
	v_mov_b64_e32 v[154:155], 0
	v_mov_b64_e32 v[156:157], 0
	v_mov_b64_e32 v[158:159], 0
	v_mov_b64_e32 v[160:161], 0
	v_mov_b64_e32 v[170:171], 0
	v_mov_b64_e32 v[172:173], 0
	v_mov_b64_e32 v[174:175], 0
	v_mov_b64_e32 v[176:177], 0
	v_mov_b64_e32 v[186:187], 0
	v_mov_b64_e32 v[188:189], 0
	v_mov_b64_e32 v[190:191], 0
	v_mov_b64_e32 v[192:193], 0
	v_mov_b64_e32 v[98:99], 0
	v_mov_b64_e32 v[100:101], 0
	v_mov_b64_e32 v[94:95], 0
	v_mov_b64_e32 v[96:97], 0
	v_mov_b64_e32 v[78:79], 0
	v_mov_b64_e32 v[80:81], 0
	v_mov_b64_e32 v[74:75], 0
	v_mov_b64_e32 v[76:77], 0
	s_mov_b32 s67, 1
	s_branch .LBB0_571

.LBB0_984:
	s_ashr_i32 s11, s10, 31
	s_lshl_b64 s[30:31], s[10:11], 18
	s_add_u32 s30, s40, s30
	s_addc_u32 s31, s41, s31
	s_and_b64 s[46:47], s[36:37], exec
	s_cselect_b32 s2, s31, s39
	s_cselect_b32 s11, s30, s38
	s_xor_b32 s44, s44, 0x400
	s_add_i32 s82, s44, 0
	s_add_i32 s82, s82, 0x23400
	s_add_u32 s85, s38, 0x100
	s_addc_u32 s86, s39, 0
	s_mov_b32 s87, -2
	s_mov_b64 s[38:39], s[18:19]
	v_mov_b64_e32 v[90:91], 0
	v_mov_b64_e32 v[92:93], 0
	v_mov_b64_e32 v[102:103], 0
	v_mov_b64_e32 v[104:105], 0
	v_mov_b64_e32 v[114:115], 0
	v_mov_b64_e32 v[116:117], 0
	v_mov_b64_e32 v[118:119], 0
	v_mov_b64_e32 v[120:121], 0
	v_mov_b64_e32 v[66:67], 0
	v_mov_b64_e32 v[68:69], 0
	v_mov_b64_e32 v[70:71], 0
	v_mov_b64_e32 v[72:73], 0
	v_mov_b64_e32 v[82:83], 0
	v_mov_b64_e32 v[84:85], 0
	v_mov_b64_e32 v[86:87], 0
	v_mov_b64_e32 v[88:89], 0
	v_mov_b64_e32 v[106:107], 0
	v_mov_b64_e32 v[108:109], 0
	v_mov_b64_e32 v[110:111], 0
	v_mov_b64_e32 v[112:113], 0
	v_mov_b64_e32 v[122:123], 0
	v_mov_b64_e32 v[124:125], 0
	v_mov_b64_e32 v[126:127], 0
	v_mov_b64_e32 v[128:129], 0
	v_mov_b64_e32 v[130:131], 0
	v_mov_b64_e32 v[132:133], 0
	v_mov_b64_e32 v[134:135], 0
	v_mov_b64_e32 v[136:137], 0
	v_mov_b64_e32 v[146:147], 0
	v_mov_b64_e32 v[148:149], 0
	v_mov_b64_e32 v[150:151], 0
	v_mov_b64_e32 v[152:153], 0
	v_mov_b64_e32 v[162:163], 0
	v_mov_b64_e32 v[164:165], 0
	v_mov_b64_e32 v[166:167], 0
	v_mov_b64_e32 v[168:169], 0
	v_mov_b64_e32 v[178:179], 0
	v_mov_b64_e32 v[180:181], 0
	v_mov_b64_e32 v[182:183], 0
	v_mov_b64_e32 v[184:185], 0
	v_mov_b64_e32 v[138:139], 0
	v_mov_b64_e32 v[140:141], 0
	v_mov_b64_e32 v[142:143], 0
	v_mov_b64_e32 v[144:145], 0
	v_mov_b64_e32 v[154:155], 0
	v_mov_b64_e32 v[156:157], 0
	v_mov_b64_e32 v[158:159], 0
	v_mov_b64_e32 v[160:161], 0
	v_mov_b64_e32 v[170:171], 0
	v_mov_b64_e32 v[172:173], 0
	v_mov_b64_e32 v[174:175], 0
	v_mov_b64_e32 v[176:177], 0
	v_mov_b64_e32 v[186:187], 0
	v_mov_b64_e32 v[188:189], 0
	v_mov_b64_e32 v[190:191], 0
	v_mov_b64_e32 v[192:193], 0
	v_mov_b64_e32 v[94:95], 0
	v_mov_b64_e32 v[96:97], 0
	v_mov_b64_e32 v[98:99], 0
	v_mov_b64_e32 v[100:101], 0
	v_mov_b64_e32 v[74:75], 0
	v_mov_b64_e32 v[76:77], 0
	v_mov_b64_e32 v[78:79], 0
	v_mov_b64_e32 v[80:81], 0
	s_mov_b32 s88, 1
	s_branch .LBB0_986

.LBB0_1080:
	s_ashr_i32 s57, s56, 31
	s_lshl_b64 s[12:13], s[56:57], 18
	s_add_u32 s12, s70, s12
	s_addc_u32 s13, s71, s13
	s_and_b64 s[28:29], s[0:1], exec
	s_cselect_b32 s57, s13, s51
	s_cselect_b32 s82, s12, s50
	s_lshl_b32 s28, s68, 8
	s_or_b32 s29, s28, 0x80
	s_add_u32 s30, s50, 0x100
	s_addc_u32 s31, s51, 0
	s_mov_b32 s34, -2
	s_mov_b64 s[78:79], s[96:97]
	v_mov_b64_e32 v[82:83], 0
	v_mov_b64_e32 v[84:85], 0
	v_mov_b64_e32 v[90:91], 0
	v_mov_b64_e32 v[92:93], 0
	v_mov_b64_e32 v[114:115], 0
	v_mov_b64_e32 v[116:117], 0
	v_mov_b64_e32 v[118:119], 0
	v_mov_b64_e32 v[120:121], 0
	v_mov_b64_e32 v[66:67], 0
	v_mov_b64_e32 v[68:69], 0
	v_mov_b64_e32 v[70:71], 0
	v_mov_b64_e32 v[72:73], 0
	v_mov_b64_e32 v[74:75], 0
	v_mov_b64_e32 v[76:77], 0
	v_mov_b64_e32 v[78:79], 0
	v_mov_b64_e32 v[80:81], 0
	v_mov_b64_e32 v[98:99], 0
	v_mov_b64_e32 v[100:101], 0
	v_mov_b64_e32 v[106:107], 0
	v_mov_b64_e32 v[108:109], 0
	v_mov_b64_e32 v[122:123], 0
	v_mov_b64_e32 v[124:125], 0
	v_mov_b64_e32 v[126:127], 0
	v_mov_b64_e32 v[128:129], 0
	v_mov_b64_e32 v[130:131], 0
	v_mov_b64_e32 v[132:133], 0
	v_mov_b64_e32 v[134:135], 0
	v_mov_b64_e32 v[136:137], 0
	v_mov_b64_e32 v[146:147], 0
	v_mov_b64_e32 v[148:149], 0
	v_mov_b64_e32 v[150:151], 0
	v_mov_b64_e32 v[152:153], 0
	v_mov_b64_e32 v[162:163], 0
	v_mov_b64_e32 v[164:165], 0
	v_mov_b64_e32 v[166:167], 0
	v_mov_b64_e32 v[168:169], 0
	v_mov_b64_e32 v[170:171], 0
	v_mov_b64_e32 v[172:173], 0
	v_mov_b64_e32 v[174:175], 0
	v_mov_b64_e32 v[176:177], 0
	v_mov_b64_e32 v[138:139], 0
	v_mov_b64_e32 v[140:141], 0
	v_mov_b64_e32 v[142:143], 0
	v_mov_b64_e32 v[144:145], 0
	v_mov_b64_e32 v[154:155], 0
	v_mov_b64_e32 v[156:157], 0
	v_mov_b64_e32 v[158:159], 0
	v_mov_b64_e32 v[160:161], 0
	v_mov_b64_e32 v[178:179], 0
	v_mov_b64_e32 v[180:181], 0
	v_mov_b64_e32 v[182:183], 0
	v_mov_b64_e32 v[184:185], 0
	v_mov_b64_e32 v[186:187], 0
	v_mov_b64_e32 v[188:189], 0
	v_mov_b64_e32 v[190:191], 0
	v_mov_b64_e32 v[192:193], 0
	v_mov_b64_e32 v[102:103], 0
	v_mov_b64_e32 v[104:105], 0
	v_mov_b64_e32 v[110:111], 0
	v_mov_b64_e32 v[112:113], 0
	v_mov_b64_e32 v[86:87], 0
	v_mov_b64_e32 v[88:89], 0
	v_mov_b64_e32 v[94:95], 0
	v_mov_b64_e32 v[96:97], 0
	s_mov_b32 s35, 1
	s_branch .LBB0_1082
